# edge kernels: four pairs of scalar softplus +1.0 adds folded into v_pk_add_f32
# baseline (speedup 1.0000x reference)
.Lprio_e0_done:
	s_mov_b32 s93, s94
	s_add_u32 s94, s94, 0x1000
	s_cmp_lt_u32 s94, 0x61a8
	s_cselect_b32 s95, s94, s93
	s_lshl_b32 s95, s95, 9
	s_add_u32 s56, s8, s95
	s_addc_u32 s57, s9, 0
	v_sub_f32_e32 v36, v32, v64
	v_fmamk_f32 v38, v36, 0x4297576a, v57
	v_fmamk_f32 v39, v36, 0x4297576a, v73
	v_med3_f32 v41, v38, s20, v71
	v_med3_f32 v43, v39, s20, v71
	v_mul_f32_e64 v38, v41, -v41
	v_mul_f32_e64 v39, v43, -v43
	v_exp_f32_e32 v38, v38
	v_exp_f32_e32 v39, v39
	v_fmamk_f32 v40, v41, 0x4019be61, v72
	v_fmamk_f32 v41, v41, 0xc019be61, v72
	v_exp_f32_e32 v42, v41
	v_pk_mul_f32 v[46:47], v[32:33], v[38:39] op_sel:[1,0]
	v_fmamk_f32 v38, v43, 0x4019be61, v72
	v_exp_f32_e32 v41, v38
	v_fmamk_f32 v38, v43, 0xc019be61, v72
	v_exp_f32_e32 v43, v38
	v_fmamk_f32 v38, v36, 0x4297576a, v74
	v_fmamk_f32 v36, v36, 0x4297576a, v75
	v_med3_f32 v45, v38, s20, v71
	v_med3_f32 v36, v36, s20, v71
	v_mul_f32_e64 v38, v45, -v45
	v_mul_f32_e64 v39, v36, -v36
	v_exp_f32_e32 v38, v38
	v_exp_f32_e32 v39, v39
	v_exp_f32_e32 v40, v40
	v_fmamk_f32 v44, v45, 0x4019be61, v72
	v_fmamk_f32 v45, v45, 0xc019be61, v72
	v_pk_mul_f32 v[54:55], v[32:33], v[38:39] op_sel:[1,0]
	v_fmamk_f32 v38, v36, 0x4019be61, v72
	v_exp_f32_e32 v48, v45
	v_exp_f32_e32 v45, v38
	v_pk_mul_f32 v[50:51], v[40:41], v[46:47]
	v_pk_mul_f32 v[38:39], v[40:41], s[14:15] op_sel_hi:[1,0]
	v_exp_f32_e32 v44, v44
	v_pk_mul_f32 v[52:53], v[38:39], v[50:51]
	v_pk_mul_f32 v[38:39], v[38:39], s[14:15] op_sel_hi:[1,0]
	ds_read_b128 v[12:15], v66
	ds_read_b128 v[8:11], v66 offset:1024
	ds_read_b128 v[4:7], v66 offset:2048
	ds_read_b128 v[0:3], v66 offset:3072
	ds_read_b128 v[16:19], v67
	ds_read_b128 v[20:23], v67 offset:32
	ds_read_b128 v[24:27], v67 offset:64
	ds_read_b128 v[28:31], v67 offset:96
	v_pk_mul_f32 v[78:79], v[38:39], v[52:53]
	v_pk_mul_f32 v[38:39], v[38:39], s[14:15] op_sel_hi:[1,0]
	v_pk_mul_f32 v[82:83], v[42:43], v[46:47]
	v_pk_mul_f32 v[80:81], v[38:39], v[78:79]
	v_pk_mul_f32 v[38:39], v[42:43], s[14:15] op_sel_hi:[1,0]
	v_pk_mul_f32 v[86:87], v[44:45], v[54:55]
	v_pk_mul_f32 v[42:43], v[38:39], v[82:83]
	v_pk_mul_f32 v[38:39], v[38:39], s[14:15] op_sel_hi:[1,0]
	v_cvt_pk_f16_f32 v40, v50, v52
	v_pk_mul_f32 v[84:85], v[38:39], v[42:43]
	v_pk_mul_f32 v[38:39], v[44:45], s[14:15] op_sel_hi:[1,0]
	v_cvt_pk_f16_f32 v41, v78, v80
	v_pk_mul_f32 v[88:89], v[38:39], v[86:87]
	v_pk_mul_f32 v[38:39], v[38:39], s[14:15] op_sel_hi:[1,0]
	v_fmamk_f32 v36, v36, 0xc019be61, v72
	v_pk_mul_f32 v[90:91], v[38:39], v[88:89]
	v_pk_mul_f32 v[44:45], v[38:39], s[14:15] op_sel_hi:[1,0]
	v_cvt_pk_f16_f32 v38, v84, v42
	v_cvt_pk_f16_f32 v39, v82, v46
	v_cvt_pk_f16_f32 v42, v85, v43
	v_cvt_pk_f16_f32 v43, v83, v47
	s_waitcnt lgkmcnt(0)
	v_mfma_f32_32x32x16_f16 v[16:31], v[12:15], v[38:41], v[16:31]
	v_mul_f32_e64 v12, v44, v90
	v_mul_f32_e64 v13, v45, v91
	v_cvt_pk_f16_f32 v44, v51, v53
	v_cvt_pk_f16_f32 v45, v79, v81
	v_exp_f32_e32 v49, v36
	ds_read_b128 v[50:53], v66 offset:4096
	v_cvt_pk_f16_f32 v82, v87, v89
	v_cvt_pk_f16_f32 v83, v91, v13
	v_mfma_f32_32x32x16_f16 v[16:31], v[8:11], v[42:45], v[16:31]
	v_mul_f32_e64 v14, v48, v54
	v_mul_f32_e64 v15, v49, v55
	v_mul_f32_e64 v48, v48, s14
	v_mul_f32_e64 v49, v49, s14
	v_cvt_pk_f16_f32 v47, v14, v54
	v_pk_mul_f32 v[8:9], v[48:49], v[14:15]
	v_pk_mul_f32 v[10:11], v[48:49], s[14:15] op_sel_hi:[1,0]
	v_cvt_pk_f16_f32 v48, v86, v88
	v_pk_mul_f32 v[10:11], v[10:11], v[8:9]
	v_cvt_pk_f16_f32 v49, v90, v12
	v_cvt_pk_f16_f32 v46, v10, v8
	v_cvt_pk_f16_f32 v80, v11, v9
	v_cvt_pk_f16_f32 v81, v15, v55
	v_mfma_f32_32x32x16_f16 v[16:31], v[4:7], v[46:49], v[16:31]
	s_nop 0
	v_add_u32_e32 v56, s6, v56
	s_nop 0
	v_mov_b32_e32 v78, v63
	v_readlane_b32 s21, v35, 0
	s_nop 0
	v_cmp_ne_u32_sdwa s[16:17], v78, v34 src0_sel:WORD_1 src1_sel:WORD_1
	v_mfma_f32_32x32x16_f16 v[16:31], v[0:3], v[80:83], v[16:31]
	ds_read_b128 v[0:3], v67 offset:128
	ds_read_b128 v[4:7], v67 offset:160
	ds_read_b128 v[8:11], v67 offset:192
	ds_read_b128 v[12:15], v67 offset:224
	ds_read_b128 v[84:87], v66 offset:5120
	s_nop 0
	s_nop 0
	s_nop 0
	s_nop 0
	s_nop 0
	s_nop 0
	s_waitcnt lgkmcnt(1)
	v_mfma_f32_32x32x16_f16 v[0:15], v[50:53], v[38:41], v[0:15]
	ds_read_b128 v[38:41], v66 offset:6144
	ds_read_b128 v[50:53], v66 offset:7168
	s_nop 0
	s_nop 0
	s_nop 2
	v_exp_f32_e32 v16, v16
	v_exp_f32_e32 v17, v17
	v_exp_f32_e32 v18, v18
	s_waitcnt lgkmcnt(2)
	v_mfma_f32_32x32x16_f16 v[0:15], v[84:87], v[42:45], v[0:15]
	v_exp_f32_e32 v19, v19
	v_exp_f32_e32 v20, v20
	v_exp_f32_e32 v21, v21
	v_exp_f32_e32 v22, v22
	v_exp_f32_e32 v23, v23
	v_pk_add_f32 v[16:17], v[16:17], 1.0 op_sel_hi:[1,0]
	v_pk_add_f32 v[18:19], v[18:19], 1.0 op_sel_hi:[1,0]
	s_waitcnt lgkmcnt(1)
	v_mfma_f32_32x32x16_f16 v[0:15], v[38:41], v[46:49], v[0:15]
	v_pk_add_f32 v[20:21], v[20:21], 1.0 op_sel_hi:[1,0]
	s_nop 0
	v_pk_add_f32 v[22:23], v[22:23], 1.0 op_sel_hi:[1,0]
	s_nop 0
	v_log_f32_e32 v16, v16
	v_log_f32_e32 v17, v17
	v_log_f32_e32 v18, v18
	v_log_f32_e32 v19, v19
	v_log_f32_e32 v20, v20
	s_waitcnt lgkmcnt(0)
	v_mfma_f32_32x32x16_f16 v[0:15], v[50:53], v[80:83], v[0:15]
	s_nop 0
	s_nop 0
	s_nop 0
	s_nop 0
	s_nop 0
	s_nop 0
	s_nop 11
	v_exp_f32_e32 v6, v6
	v_exp_f32_e32 v7, v7
	v_exp_f32_e32 v0, v0
	v_exp_f32_e32 v1, v1
	v_log_f32_e32 v21, v21
	v_pk_add_f32 v[6:7], v[6:7], 1.0 op_sel_hi:[1,0]
	v_log_f32_e32 v22, v22
	v_log_f32_e32 v6, v6
	v_log_f32_e32 v7, v7
	v_log_f32_e32 v23, v23
	s_nop 0
	s_nop 0
	v_exp_f32_e32 v4, v4
	v_exp_f32_e32 v5, v5
	s_nop 0
	v_exp_f32_e32 v2, v2
	v_exp_f32_e32 v3, v3
	s_mov_b64 vcc, 0
	v_pk_add_f32 v[0:1], v[0:1], 1.0 op_sel_hi:[1,0]
	v_pk_mul_f32 v[6:7], v[32:33], v[6:7] op_sel:[1,0]
	s_nop 0
	s_nop 0
	v_log_f32_e32 v0, v0
	v_log_f32_e32 v1, v1
	v_cvt_pk_f16_f32 v55, v6, v7
	s_nop 0
	s_nop 0
	s_nop 0
	s_nop 0
	v_pk_mul_f32 v[16:17], v[32:33], v[16:17] op_sel:[1,0]
	v_pk_mul_f32 v[18:19], v[32:33], v[18:19] op_sel:[1,0]
	v_pk_mul_f32 v[20:21], v[32:33], v[20:21] op_sel:[1,0]
	v_pk_mul_f32 v[22:23], v[32:33], v[22:23] op_sel:[1,0]
	v_pk_add_f32 v[4:5], v[4:5], 1.0 op_sel_hi:[1,0]
	v_exp_f32_e32 v6, v10
	v_exp_f32_e32 v7, v11
	s_nop 0
	global_load_dwordx4 v[40:43], v94, s[56:57]
	global_load_dword v63, v94, s[56:57] offset:24
	global_load_dword v76, v94, s[56:57] offset:-8
	v_cvt_pk_f16_f32 v47, v22, v23
	v_cvt_pk_f16_f32 v46, v20, v21
	v_cvt_pk_f16_f32 v45, v18, v19
	v_cvt_pk_f16_f32 v44, v16, v17
	s_nop 0
	s_nop 0
	s_nop 0
	s_nop 0
	s_nop 0
	s_nop 0
	s_nop 0
	s_nop 0
	v_pk_add_f32 v[2:3], v[2:3], 1.0 op_sel_hi:[1,0]
	v_log_f32_e32 v4, v4
	v_log_f32_e32 v5, v5
	s_nop 0
	s_nop 0
	v_exp_f32_e32 v16, v24
	v_exp_f32_e32 v17, v25
	v_exp_f32_e32 v18, v26
	v_exp_f32_e32 v19, v27
	v_exp_f32_e32 v20, v28
	v_exp_f32_e32 v21, v29
	v_exp_f32_e32 v22, v30
	v_exp_f32_e32 v23, v31
	v_log_f32_e32 v2, v2
	v_log_f32_e32 v3, v3
	v_exp_f32_e32 v8, v8
	v_exp_f32_e32 v9, v9
	v_pk_mul_f32 v[0:1], v[32:33], v[0:1] op_sel:[1,0]
	v_pk_mul_f32 v[4:5], v[32:33], v[4:5] op_sel:[1,0]
	v_cvt_pk_f16_f32 v52, v0, v1
	v_pk_add_f32 v[0:1], v[6:7], 1.0 op_sel_hi:[1,0]
	v_pk_add_f32 v[16:17], v[16:17], 1.0 op_sel_hi:[1,0]
	v_log_f32_e32 v10, v0
	s_nop 0
	v_pk_add_f32 v[18:19], v[18:19], 1.0 op_sel_hi:[1,0]
	v_pk_add_f32 v[20:21], v[20:21], 1.0 op_sel_hi:[1,0]
	v_pk_add_f32 v[22:23], v[22:23], 1.0 op_sel_hi:[1,0]
	v_pk_mul_f32 v[2:3], v[32:33], v[2:3] op_sel:[1,0]
	v_cvt_pk_f16_f32 v54, v4, v5
	v_pk_add_f32 v[4:5], v[8:9], 1.0 op_sel_hi:[1,0]
	v_exp_f32_e32 v12, v12
	s_nop 0
	v_log_f32_e32 v16, v16
	v_log_f32_e32 v17, v17
	v_log_f32_e32 v18, v18
	v_log_f32_e32 v19, v19
	v_log_f32_e32 v20, v20
	v_log_f32_e32 v21, v21
	v_log_f32_e32 v22, v22
	v_log_f32_e32 v23, v23
	v_log_f32_e32 v4, v4
	v_log_f32_e32 v5, v5
	v_cvt_pk_f16_f32 v53, v2, v3
	v_log_f32_e32 v11, v1
	v_exp_f32_e32 v13, v13
	ds_read_b128 v[0:3], v68
	v_pk_mul_f32 v[16:17], v[32:33], v[16:17] op_sel:[1,0]
	v_pk_mul_f32 v[18:19], v[32:33], v[18:19] op_sel:[1,0]
	v_pk_mul_f32 v[20:21], v[32:33], v[20:21] op_sel:[1,0]
	v_pk_mul_f32 v[22:23], v[32:33], v[22:23] op_sel:[1,0]
	v_pk_mul_f32 v[8:9], v[32:33], v[4:5] op_sel:[1,0]
	s_nop 0
	v_cvt_pk_f16_f32 v51, v22, v23
	v_cvt_pk_f16_f32 v50, v20, v21
	v_cvt_pk_f16_f32 v49, v18, v19
	v_cvt_pk_f16_f32 v48, v16, v17
	v_exp_f32_e32 v14, v14
	ds_read_b128 v[4:7], v68 offset:1024
	s_waitcnt lgkmcnt(1)
	v_mfma_f32_32x32x16_f16 v[16:31], v[44:47], v[0:3], 0
	s_nop 0
	v_pk_add_f32 v[0:1], v[12:13], 1.0 op_sel_hi:[1,0]
	s_nop 0
	v_exp_f32_e32 v15, v15
	v_log_f32_e32 v0, v0
	v_log_f32_e32 v1, v1
	v_pk_mul_f32 v[10:11], v[32:33], v[10:11] op_sel:[1,0]
	v_pk_add_f32 v[2:3], v[14:15], 1.0 op_sel_hi:[1,0]
	s_waitcnt lgkmcnt(0)
	v_mfma_f32_32x32x16_f16 v[16:31], v[48:51], v[4:7], v[16:31]
	v_log_f32_e32 v12, v2
	v_log_f32_e32 v13, v3
	v_pk_mul_f32 v[4:5], v[32:33], v[0:1] op_sel:[1,0]
	ds_read_b128 v[0:3], v68 offset:2048
	v_cvt_pk_f16_f32 v82, v4, v5
	v_pk_mul_f32 v[6:7], v[32:33], v[12:13] op_sel:[1,0]
	v_cvt_pk_f16_f32 v81, v10, v11
	v_cvt_pk_f16_f32 v83, v6, v7
	ds_read_b128 v[4:7], v68 offset:3072
	s_waitcnt lgkmcnt(1)
	v_mfma_f32_32x32x16_f16 v[16:31], v[52:55], v[0:3], v[16:31]
	v_cvt_pk_f16_f32 v80, v8, v9
	v_cvt_f16_f32_e32 v0, v33
	v_mov_b32_e32 v38, v37
	v_mov_b32_e32 v39, v37
	ds_read_b128 v[84:87], v69 offset:1024
	v_cndmask_b32_e64 v0, 0, v0, s[0:1]
	v_pack_b32_f16 v36, v0, 0
	s_waitcnt lgkmcnt(1)
	v_mfma_f32_32x32x16_f16 v[16:31], v[80:83], v[4:7], v[16:31]
	ds_read_b128 v[0:3], v69
	ds_read_b128 v[88:91], v68 offset:5120
	s_ashr_i32 s17, s21, 9
	v_readlane_b32 s22, v35, 1
	s_and_b32 s17, s17, 0xffffff80
	v_or_b32_e32 v32, s17, v70
	s_ashr_i32 s17, s22, 9
	s_waitcnt lgkmcnt(1)
	v_mfma_f32_32x32x16_f16 v[16:31], v[36:39], v[0:3], v[16:31]
	ds_read_b128 v[0:3], v68 offset:4096
	v_readlane_b32 s23, v35, 2
	s_and_b32 s17, s17, 0xffffff80
	v_or_b32_e32 v33, s17, v70
	s_ashr_i32 s17, s23, 9
	v_readlane_b32 s24, v35, 3
	s_and_b32 s17, s17, 0xffffff80
	s_waitcnt lgkmcnt(0)
	v_mfma_f32_32x32x16_f16 v[0:15], v[44:47], v[0:3], 0
	ds_read_b128 v[44:47], v68 offset:6144
	v_readlane_b32 s25, v35, 4
	v_readlane_b32 s26, v35, 5
	v_readlane_b32 s27, v35, 6
	v_readlane_b32 s28, v35, 7
	v_readlane_b32 s29, v35, 8
	v_readlane_b32 s30, v35, 9
	v_mfma_f32_32x32x16_f16 v[0:15], v[48:51], v[88:91], v[0:15]
	ds_read_b128 v[48:51], v68 offset:7168
	v_readlane_b32 s31, v35, 10
	v_readlane_b32 s33, v35, 11
	v_readlane_b32 s34, v35, 12
	v_readlane_b32 s35, v35, 13
	v_readlane_b32 s36, v35, 14
	v_readlane_b32 s37, v35, 15
	s_waitcnt lgkmcnt(1)
	v_mfma_f32_32x32x16_f16 v[0:15], v[52:55], v[44:47], v[0:15]
	v_readlane_b32 s38, v35, 16
	v_readlane_b32 s39, v35, 17
	v_readlane_b32 s40, v35, 18
	v_readlane_b32 s41, v35, 19
	v_readlane_b32 s42, v35, 20
	v_readlane_b32 s43, v35, 21
	v_readlane_b32 s44, v35, 22
	s_waitcnt lgkmcnt(0)
	v_mfma_f32_32x32x16_f16 v[0:15], v[80:83], v[48:51], v[0:15]
	v_readlane_b32 s45, v35, 23
	v_readlane_b32 s46, v35, 24
	v_readlane_b32 s47, v35, 25
	v_readlane_b32 s48, v35, 26
	v_readlane_b32 s49, v35, 27
	v_readlane_b32 s50, v35, 28
	v_readlane_b32 s51, v35, 29
	v_readlane_b32 s52, v35, 30
	v_readlane_b32 s4, v35, 31
	v_or_b32_e32 v35, s17, v70
	s_ashr_i32 s17, s24, 9
	s_and_b32 s17, s17, 0xffffff80
	v_mfma_f32_32x32x16_f16 v[0:15], v[36:39], v[84:87], v[0:15]
	v_or_b32_e32 v36, s17, v70
	s_ashr_i32 s17, s25, 9
	s_and_b32 s17, s17, 0xffffff80
	v_or_b32_e32 v38, s17, v70
	s_ashr_i32 s17, s26, 9
	s_and_b32 s17, s17, 0xffffff80
	v_or_b32_e32 v39, s17, v70
	s_ashr_i32 s17, s27, 9
	s_and_b32 s17, s17, 0xffffff80
	v_or_b32_e32 v44, s17, v70
	s_ashr_i32 s17, s28, 9
	s_and_b32 s17, s17, 0xffffff80
	v_or_b32_e32 v45, s17, v70
	s_ashr_i32 s17, s29, 9
	s_and_b32 s17, s17, 0xffffff80
	ds_read_u16 v32, v32
	ds_read_u16 v91, v33
	ds_read_u16 v90, v35
	ds_read_u16 v89, v36
	ds_read_u16 v88, v38
	ds_read_u16 v87, v39
	ds_read_u16 v86, v44
	ds_read_u16 v85, v45
	v_or_b32_e32 v33, s17, v70
	s_ashr_i32 s17, s30, 9
	s_and_b32 s17, s17, 0xffffff80
	v_or_b32_e32 v35, s17, v70
	s_ashr_i32 s17, s31, 9
	s_and_b32 s17, s17, 0xffffff80
	v_or_b32_e32 v36, s17, v70
	s_ashr_i32 s17, s33, 9
	s_and_b32 s17, s17, 0xffffff80
	v_or_b32_e32 v38, s17, v70
	s_ashr_i32 s17, s34, 9
	s_and_b32 s17, s17, 0xffffff80
	v_or_b32_e32 v39, s17, v70
	s_ashr_i32 s17, s35, 9
	s_and_b32 s17, s17, 0xffffff80
	v_or_b32_e32 v44, s17, v70
	s_ashr_i32 s17, s36, 9
	s_and_b32 s17, s17, 0xffffff80
	v_or_b32_e32 v45, s17, v70
	s_ashr_i32 s17, s37, 9
	s_and_b32 s17, s17, 0xffffff80
	v_or_b32_e32 v46, s17, v70
	s_ashr_i32 s17, s38, 9
	s_and_b32 s17, s17, 0xffffff80
	v_cmp_ne_u32_sdwa s[18:19], v77, v34 src0_sel:DWORD src1_sel:WORD_1
	ds_read_u16 v84, v33
	ds_read_u16 v83, v35
	ds_read_u16 v82, v36
	ds_read_u16 v81, v38
	ds_read_u16 v80, v39
	ds_read_u16 v79, v44
	ds_read_u16 v78, v45
	ds_read_u16 v77, v46
	v_or_b32_e32 v33, s17, v70
	s_ashr_i32 s17, s39, 9
	s_and_b32 s17, s17, 0xffffff80
	v_or_b32_e32 v35, s17, v70
	s_ashr_i32 s17, s40, 9
	s_and_b32 s17, s17, 0xffffff80
	v_or_b32_e32 v36, s17, v70
	s_ashr_i32 s17, s41, 9
	s_and_b32 s17, s17, 0xffffff80
	v_or_b32_e32 v38, s17, v70
	s_ashr_i32 s17, s42, 9
	s_and_b32 s17, s17, 0xffffff80
	v_or_b32_e32 v39, s17, v70
	s_ashr_i32 s17, s43, 9
	s_and_b32 s17, s17, 0xffffff80
	v_or_b32_e32 v44, s17, v70
	s_ashr_i32 s17, s44, 9
	s_and_b32 s17, s17, 0xffffff80
	v_or_b32_e32 v45, s17, v70
	s_ashr_i32 s17, s45, 9
	s_and_b32 s17, s17, 0xffffff80
	v_or_b32_e32 v46, s17, v70
	s_ashr_i32 s17, s46, 9
	s_and_b32 s17, s17, 0xffffff80
	ds_read_u16 v55, v33
	ds_read_u16 v54, v35
	ds_read_u16 v53, v36
	ds_read_u16 v52, v38
	ds_read_u16 v51, v39
	ds_read_u16 v50, v44
	ds_read_u16 v49, v45
	ds_read_u16 v48, v46
	v_or_b32_e32 v33, s17, v70
	s_ashr_i32 s17, s47, 9
	s_and_b32 s17, s17, 0xffffff80
	v_or_b32_e32 v35, s17, v70
	s_ashr_i32 s17, s48, 9
	s_and_b32 s17, s17, 0xffffff80
	v_or_b32_e32 v36, s17, v70
	s_ashr_i32 s17, s49, 9
	s_and_b32 s17, s17, 0xffffff80
	v_or_b32_e32 v38, s17, v70
	s_ashr_i32 s17, s50, 9
	s_and_b32 s17, s17, 0xffffff80
	v_or_b32_e32 v39, s17, v70
	s_ashr_i32 s17, s51, 9
	s_and_b32 s17, s17, 0xffffff80
	v_or_b32_e32 v92, s17, v70
	s_ashr_i32 s17, s52, 9
	s_and_b32 s17, s17, 0xffffff80
	v_or_b32_e32 v93, s17, v70
	ds_read_u16 v47, v33
	ds_read_u16 v46, v35
	ds_read_u16 v45, v36
	ds_read_u16 v44, v38
	ds_read_u16 v39, v39
	ds_read_u16 v38, v92
	ds_read_u16 v36, v93
	s_ashr_i32 s4, s4, 9
	s_and_b32 s4, s4, 0xffffff80
	s_waitcnt lgkmcnt(14)
	v_cvt_f32_f16_e32 v32, v32
	v_or_b32_e32 v33, s4, v70
	ds_read_u16 v35, v33
	s_waitcnt vmcnt(0)
	v_permlane32_swap_b32_e32 v16, v0
	s_bitcmp1_b32 s18, 0
	v_mul_f32_e32 v32, v16, v32
	v_mov_b32_e32 v33, v16
	v_cmp_lt_i32_e64 s[2:3], s7, v56
	v_permlane32_swap_b32_e32 v17, v1
	v_permlane32_swap_b32_e32 v18, v2
	v_permlane32_swap_b32_e32 v19, v3
	v_permlane32_swap_b32_e32 v20, v4
	v_permlane32_swap_b32_e32 v21, v5
	v_permlane32_swap_b32_e32 v22, v6
	v_permlane32_swap_b32_e32 v23, v7
	v_permlane32_swap_b32_e32 v24, v8
	v_permlane32_swap_b32_e32 v25, v9
	v_permlane32_swap_b32_e32 v26, v10
	v_permlane32_swap_b32_e32 v27, v11
	v_permlane32_swap_b32_e32 v28, v12
	v_permlane32_swap_b32_e32 v29, v13
	v_permlane32_swap_b32_e32 v30, v14
	v_permlane32_swap_b32_e32 v31, v15
	s_cselect_b64 s[18:19], -1, 0
	s_bitcmp0_b32 s16, 0
	v_pk_add_f32 v[32:33], v[32:33], 0 op_sel_hi:[1,0]
	s_cbranch_scc1 .LBB3_13
	v_readlane_b32 s4, v34, 0
	s_bfe_u32 s17, s4, 0x80008
	v_lshl_or_b32 v16, s17, 7, v70
	ds_read_u16 v16, v16
	s_bfe_u32 s4, s4, 0x100010
	s_lshl_b32 s4, s4, 8
	s_add_u32 s58, s60, s4
	s_addc_u32 s59, s61, 0
	s_cmp_lg_u64 s[18:19], 0
	s_cselect_b32 s58, s58, s62
	s_cselect_b32 s59, s59, s63
	s_nop 0
	s_waitcnt lgkmcnt(0)
	v_fma_mix_f32 v16, v16, v33, v32 op_sel_hi:[1,0,0]
	v_mov_b64_e32 v[32:33], 0
	s_nop 0
	s_mov_b64 s[18:19], -1
	s_nop 0
	global_store_dword v95, v16, s[58:59] sc1

.Lprio_e1_done:
	s_mov_b32 s93, s94
	s_add_u32 s94, s94, 0x1000
	s_cmp_lt_u32 s94, 0x61a8
	s_cselect_b32 s95, s94, s93
	s_lshl_b32 s95, s95, 9
	s_add_u32 s56, s8, s95
	s_addc_u32 s57, s9, 0
	ds_bpermute_b32 v126, v125, v51
	v_sub_f32_e32 v39, v48, v67
	v_fmamk_f32 v32, v39, 0x4297576a, v65
	v_fmamk_f32 v33, v39, 0x4297576a, v76
	v_med3_f32 v35, v32, s22, v74
	v_med3_f32 v37, v33, s22, v74
	v_mul_f32_e64 v32, v35, -v35
	v_fmamk_f32 v34, v35, 0x4019be61, v75
	v_mul_f32_e64 v33, v37, -v37
	v_fmamk_f32 v35, v35, 0xc019be61, v75
	v_exp_f32_e32 v32, v32
	v_exp_f32_e32 v33, v33
	v_exp_f32_e32 v36, v35
	v_fmamk_f32 v35, v37, 0x4019be61, v75
	v_exp_f32_e32 v34, v34
	v_exp_f32_e32 v35, v35
	v_fmamk_f32 v37, v37, 0xc019be61, v75
	v_exp_f32_e32 v37, v37
	v_pk_mul_f32 v[32:33], v[48:49], v[32:33] op_sel:[1,0]
	ds_read_b128 v[28:31], v69
	ds_read_b128 v[24:27], v69 offset:1024
	ds_read_b128 v[20:23], v69 offset:2048
	ds_read_b128 v[16:19], v69 offset:3072
	ds_read_b128 v[0:3], v70
	ds_read_b128 v[4:7], v70 offset:32
	ds_read_b128 v[8:11], v70 offset:64
	ds_read_b128 v[12:15], v70 offset:96
	v_pk_mul_f32 v[44:45], v[34:35], v[32:33]
	v_pk_mul_f32 v[34:35], v[34:35], s[16:17] op_sel_hi:[1,0]
	v_mov_b32_e32 v99, v80
	v_fmamk_f32 v38, v39, 0x4297576a, v77
	v_fmamk_f32 v39, v39, 0x4297576a, v78
	v_pk_mul_f32 v[46:47], v[34:35], v[44:45]
	v_pk_mul_f32 v[34:35], v[34:35], s[16:17] op_sel_hi:[1,0]
	v_pk_mul_f32 v[80:81], v[36:37], v[32:33]
	v_pk_mul_f32 v[36:37], v[36:37], s[16:17] op_sel_hi:[1,0]
	v_med3_f32 v41, v38, s22, v74
	v_med3_f32 v43, v39, s22, v74
	v_pk_mul_f32 v[58:59], v[34:35], v[46:47]
	v_pk_mul_f32 v[34:35], v[34:35], s[16:17] op_sel_hi:[1,0]
	v_pk_mul_f32 v[82:83], v[36:37], v[80:81]
	v_pk_mul_f32 v[36:37], v[36:37], s[16:17] op_sel_hi:[1,0]
	v_mul_f32_e64 v38, v41, -v41
	v_fmamk_f32 v40, v41, 0x4019be61, v75
	v_mul_f32_e64 v39, v43, -v43
	v_fmamk_f32 v41, v41, 0xc019be61, v75
	v_pk_mul_f32 v[34:35], v[34:35], v[58:59]
	v_pk_mul_f32 v[36:37], v[36:37], v[82:83]
	v_exp_f32_e32 v38, v38
	v_exp_f32_e32 v39, v39
	v_exp_f32_e32 v42, v41
	v_fmamk_f32 v41, v43, 0x4019be61, v75
	v_cvt_pk_f16_f32 v56, v44, v46
	v_cvt_pk_f16_f32 v54, v36, v82
	v_cvt_pk_f16_f32 v57, v58, v34
	v_cvt_pk_f16_f32 v55, v80, v32
	v_exp_f32_e32 v40, v40
	v_exp_f32_e32 v41, v41
	s_waitcnt lgkmcnt(0)
	v_mfma_f32_32x32x16_f16 v[0:15], v[28:31], v[54:57], v[0:15]
	v_mul_f32_e64 v38, v49, v38
	v_mul_f32_e64 v39, v49, v39
	v_fmamk_f32 v43, v43, 0xc019be61, v75
	v_mul_f32_e64 v84, v40, v38
	v_mul_f32_e64 v85, v41, v39
	v_pk_mul_f32 v[40:41], v[40:41], s[16:17] op_sel_hi:[1,0]
	v_cvt_pk_f16_f32 v30, v45, v47
	v_pk_mul_f32 v[86:87], v[40:41], v[84:85]
	v_pk_mul_f32 v[28:29], v[40:41], s[16:17] op_sel_hi:[1,0]
	v_cvt_pk_f16_f32 v31, v59, v35
	v_pk_mul_f32 v[40:41], v[28:29], v[86:87]
	v_pk_mul_f32 v[28:29], v[28:29], s[16:17] op_sel_hi:[1,0]
	v_exp_f32_e32 v43, v43
	v_pk_mul_f32 v[88:89], v[28:29], v[40:41]
	v_cvt_pk_f16_f32 v28, v37, v83
	v_cvt_pk_f16_f32 v29, v81, v33
	v_pk_mul_f32 v[36:37], v[42:43], v[38:39]
	v_pk_mul_f32 v[42:43], v[42:43], s[16:17] op_sel_hi:[1,0]
	v_mfma_f32_32x32x16_f16 v[0:15], v[24:27], v[28:31], v[0:15]
	v_mul_f32_e64 v32, v42, v36
	v_mul_f32_e64 v33, v43, v37
	v_mul_f32_e64 v24, v42, s16
	v_mul_f32_e64 v25, v43, s16
	v_cvt_pk_f16_f32 v26, v84, v86
	v_pk_mul_f32 v[34:35], v[24:25], v[32:33]
	v_cvt_pk_f16_f32 v27, v40, v88
	v_cvt_pk_f16_f32 v24, v34, v32
	v_cvt_pk_f16_f32 v25, v36, v38
	v_cvt_pk_f16_f32 v84, v85, v87
	v_cvt_pk_f16_f32 v82, v35, v33
	v_mfma_f32_32x32x16_f16 v[0:15], v[20:23], v[24:27], v[0:15]
	ds_read_b128 v[20:23], v69 offset:4096
	v_cvt_pk_f16_f32 v85, v41, v89
	v_cvt_pk_f16_f32 v83, v37, v39
	ds_read_b128 v[32:35], v70 offset:128
	ds_read_b128 v[36:39], v70 offset:160
	ds_read_b128 v[40:43], v70 offset:192
	ds_read_b128 v[44:47], v70 offset:224
	s_nop 0
	v_add_u32_e32 v64, s12, v64
	v_perm_b32 v127, v126, v51, s64
	s_nop 0
	v_readlane_b32 s70, v127, 0
	v_readlane_b32 s71, v127, 1
	v_readlane_b32 s72, v127, 2
	v_readlane_b32 s73, v127, 3
	v_readlane_b32 s74, v127, 4
	v_readlane_b32 s75, v127, 5
	v_readlane_b32 s76, v127, 6
	v_readlane_b32 s77, v127, 7
	v_readlane_b32 s78, v127, 8
	v_readlane_b32 s79, v127, 9
	v_readlane_b32 s80, v127, 10
	v_readlane_b32 s81, v127, 11
	v_readlane_b32 s82, v127, 12
	v_readlane_b32 s83, v127, 13
	v_readlane_b32 s84, v127, 14
	v_readlane_b32 s85, v127, 15
	s_pack_ll_b32_b16 s48, s70, 0
	v_mfma_f32_32x32x16_f16 v[0:15], v[16:19], v[82:85], v[0:15]
	ds_read_b128 v[16:19], v69 offset:5120
	s_nop 0
	s_lshl_b32 s48, s48, 8
	s_and_b32 s48, s48, 0xffff00
	s_pack_ll_b32_b16 s47, s71, 0
	s_add_u32 s48, s4, s48
	s_addc_u32 s49, s5, 0
	s_waitcnt lgkmcnt(1)
	v_mfma_f32_32x32x16_f16 v[32:47], v[20:23], v[54:57], v[32:47]
	ds_read_b128 v[20:23], v69 offset:6144
	s_lshl_b32 s47, s47, 8
	s_and_b32 s47, s47, 0xffff00
	s_pack_ll_b32_b16 s46, s72, 0
	s_pack_ll_b32_b16 s45, s73, 0
	s_pack_ll_b32_b16 s44, s74, 0
	s_pack_ll_b32_b16 s43, s75, 0
	s_waitcnt lgkmcnt(1)
	v_mfma_f32_32x32x16_f16 v[32:47], v[16:19], v[28:31], v[32:47]
	s_nop 0
	s_nop 0
	s_mov_b64 vcc, 0
	s_nop 0
	s_nop 0
	s_pack_ll_b32_b16 s3, s76, 0
	s_pack_ll_b32_b16 s2, s77, 0
	s_waitcnt lgkmcnt(0)
	v_mfma_f32_32x32x16_f16 v[32:47], v[20:23], v[24:27], v[32:47]
	s_nop 0
	s_nop 0
	s_pack_ll_b32_b16 s36, s78, 0
	s_pack_ll_b32_b16 s35, s79, 0
	s_pack_ll_b32_b16 s34, s80, 0
	s_pack_ll_b32_b16 s33, s81, 0
	s_pack_ll_b32_b16 s31, s82, 0
	s_pack_ll_b32_b16 s30, s83, 0
	s_pack_ll_b32_b16 s29, s84, 0
	s_pack_ll_b32_b16 s28, s85, 0
	s_pack_hh_b32_b16 s27, s70, 0
	s_pack_hh_b32_b16 s26, s71, 0
	s_pack_hh_b32_b16 s25, s72, 0
	s_pack_hh_b32_b16 s24, s73, 0
	s_pack_hh_b32_b16 s23, s74, 0
	s_pack_hh_b32_b16 s42, s75, 0
	s_pack_hh_b32_b16 s41, s76, 0
	s_pack_hh_b32_b16 s40, s77, 0
	s_pack_hh_b32_b16 s39, s78, 0
	s_pack_hh_b32_b16 s38, s79, 0
	s_pack_hh_b32_b16 s37, s80, 0
	s_pack_hh_b32_b16 s21, s81, 0
	s_pack_hh_b32_b16 s20, s82, 0
	s_pack_hh_b32_b16 s19, s83, 0
	s_pack_hh_b32_b16 s18, s84, 0
	s_pack_hh_b32_b16 s10, s85, 0
	ds_read_b128 v[16:19], v69 offset:7168
	s_nop 0
	global_load_dwordx4 v[56:59], v124, s[56:57]
	global_load_dword v80, v124, s[56:57] offset:24
	global_load_dword v51, v124, s[56:57] offset:-8
	global_load_dword v112, v79, s[48:49]
	s_add_u32 s48, s4, s47
	s_addc_u32 s49, s5, 0
	s_lshl_b32 s46, s46, 8
	s_and_b32 s46, s46, 0xffff00
	s_add_u32 s46, s4, s46
	s_addc_u32 s47, s5, 0
	s_lshl_b32 s45, s45, 8
	s_and_b32 s45, s45, 0xffff00
	global_load_dword v110, v79, s[48:49]
	global_load_dword v108, v79, s[46:47]
	s_add_u32 s46, s4, s45
	s_addc_u32 s47, s5, 0
	s_lshl_b32 s44, s44, 8
	s_and_b32 s44, s44, 0xffff00
	s_add_u32 s44, s4, s44
	s_addc_u32 s45, s5, 0
	s_lshl_b32 s43, s43, 8
	s_and_b32 s43, s43, 0xffff00
	global_load_dword v106, v79, s[46:47]
	global_load_dword v104, v79, s[44:45]
	s_add_u32 s44, s4, s43
	s_addc_u32 s45, s5, 0
	s_lshl_b32 s3, s3, 8
	s_and_b32 s3, s3, 0xffff00
	global_load_dword v102, v79, s[44:45]
	s_add_u32 s44, s4, s3
	s_addc_u32 s45, s5, 0
	s_lshl_b32 s2, s2, 8
	s_and_b32 s2, s2, 0xffff00
	s_add_u32 s2, s4, s2
	global_load_dword v100, v79, s[44:45]
	s_addc_u32 s3, s5, 0
	global_load_dword v114, v79, s[2:3]
	s_lshl_b32 s2, s36, 8
	s_and_b32 s2, s2, 0xffff00
	s_add_u32 s2, s4, s2
	s_addc_u32 s3, s5, 0
	global_load_dword v113, v79, s[2:3]
	s_lshl_b32 s2, s35, 8
	s_and_b32 s2, s2, 0xffff00
	s_add_u32 s2, s4, s2
	s_addc_u32 s3, s5, 0
	global_load_dword v111, v79, s[2:3]
	s_lshl_b32 s2, s34, 8
	s_and_b32 s2, s2, 0xffff00
	s_add_u32 s2, s4, s2
	s_addc_u32 s3, s5, 0
	global_load_dword v109, v79, s[2:3]
	s_lshl_b32 s2, s33, 8
	s_and_b32 s2, s2, 0xffff00
	s_add_u32 s2, s4, s2
	s_addc_u32 s3, s5, 0
	global_load_dword v107, v79, s[2:3]
	s_lshl_b32 s2, s31, 8
	s_and_b32 s2, s2, 0xffff00
	s_add_u32 s2, s4, s2
	s_addc_u32 s3, s5, 0
	global_load_dword v105, v79, s[2:3]
	s_lshl_b32 s2, s30, 8
	s_and_b32 s2, s2, 0xffff00
	s_add_u32 s2, s4, s2
	s_addc_u32 s3, s5, 0
	global_load_dword v103, v79, s[2:3]
	s_lshl_b32 s2, s29, 8
	s_and_b32 s2, s2, 0xffff00
	s_add_u32 s2, s4, s2
	s_addc_u32 s3, s5, 0
	global_load_dword v101, v79, s[2:3]
	s_lshl_b32 s2, s28, 8
	s_and_b32 s2, s2, 0xffff00
	s_add_u32 s2, s4, s2
	s_addc_u32 s3, s5, 0
	global_load_dword v98, v79, s[2:3]
	s_lshl_b32 s2, s27, 8
	s_and_b32 s2, s2, 0xffff00
	s_add_u32 s2, s4, s2
	s_addc_u32 s3, s5, 0
	global_load_dword v97, v79, s[2:3]
	s_lshl_b32 s2, s26, 8
	s_and_b32 s2, s2, 0xffff00
	s_add_u32 s2, s4, s2
	s_addc_u32 s3, s5, 0
	global_load_dword v96, v79, s[2:3]
	s_lshl_b32 s2, s25, 8
	s_and_b32 s2, s2, 0xffff00
	s_add_u32 s2, s4, s2
	s_addc_u32 s3, s5, 0
	global_load_dword v94, v79, s[2:3]
	s_lshl_b32 s2, s24, 8
	s_and_b32 s2, s2, 0xffff00
	s_add_u32 s2, s4, s2
	s_addc_u32 s3, s5, 0
	global_load_dword v91, v79, s[2:3]
	s_lshl_b32 s2, s23, 8
	s_and_b32 s2, s2, 0xffff00
	s_add_u32 s2, s4, s2
	s_addc_u32 s3, s5, 0
	global_load_dword v93, v79, s[2:3]
	s_lshl_b32 s2, s42, 8
	s_and_b32 s2, s2, 0xffff00
	s_add_u32 s2, s4, s2
	s_addc_u32 s3, s5, 0
	global_load_dword v90, v79, s[2:3]
	s_lshl_b32 s2, s41, 8
	s_and_b32 s2, s2, 0xffff00
	s_add_u32 s2, s4, s2
	s_addc_u32 s3, s5, 0
	global_load_dword v88, v79, s[2:3]
	s_lshl_b32 s2, s40, 8
	s_and_b32 s2, s2, 0xffff00
	s_add_u32 s2, s4, s2
	s_addc_u32 s3, s5, 0
	global_load_dword v86, v79, s[2:3]
	s_lshl_b32 s2, s39, 8
	s_and_b32 s2, s2, 0xffff00
	s_nop 0
	s_nop 0
	s_add_u32 s2, s4, s2
	s_waitcnt lgkmcnt(0)
	v_mfma_f32_32x32x16_f16 v[32:47], v[16:19], v[82:85], v[32:47]
	v_exp_f32_e32 v0, v0
	v_exp_f32_e32 v1, v1
	s_addc_u32 s3, s5, 0
	global_load_dword v85, v79, s[2:3]
	s_lshl_b32 s2, s38, 8
	s_and_b32 s2, s2, 0xffff00
	s_nop 0
	s_nop 0
	s_add_u32 s2, s4, s2
	v_exp_f32_e32 v6, v6
	v_exp_f32_e32 v7, v7
	s_addc_u32 s3, s5, 0
	global_load_dword v83, v79, s[2:3]
	s_lshl_b32 s2, s37, 8
	s_and_b32 s2, s2, 0xffff00
	s_add_u32 s2, s4, s2
	s_addc_u32 s3, s5, 0
	global_load_dword v92, v79, s[2:3]
	s_lshl_b32 s2, s21, 8
	s_and_b32 s2, s2, 0xffff00
	s_add_u32 s2, s4, s2
	s_addc_u32 s3, s5, 0
	global_load_dword v89, v79, s[2:3]
	s_lshl_b32 s2, s20, 8
	s_and_b32 s2, s2, 0xffff00
	s_add_u32 s2, s4, s2
	s_addc_u32 s3, s5, 0
	s_lshl_b32 s19, s19, 8
	s_and_b32 s19, s19, 0xffff00
	s_add_u32 s20, s4, s19
	s_addc_u32 s21, s5, 0
	s_lshl_b32 s18, s18, 8
	s_and_b32 s18, s18, 0xffff00
	s_add_u32 s18, s4, s18
	s_addc_u32 s19, s5, 0
	s_lshl_b32 s10, s10, 8
	s_and_b32 s10, s10, 0xffff00
	s_add_u32 s24, s4, s10
	s_addc_u32 s25, s5, 0
	global_load_dword v87, v79, s[2:3]
	global_load_dword v84, v79, s[20:21]
	global_load_dword v82, v79, s[18:19]
	global_load_dword v81, v79, s[24:25]
	v_pk_add_f32 v[0:1], v[0:1], 1.0 op_sel_hi:[1,0]
	s_nop 0
	s_nop 0
	v_exp_f32_e32 v16, v4
	v_exp_f32_e32 v17, v5
	v_log_f32_e32 v4, v0
	v_log_f32_e32 v5, v1
	s_nop 0
	s_nop 0
	v_exp_f32_e32 v2, v2
	v_exp_f32_e32 v3, v3
	v_pk_add_f32 v[6:7], v[6:7], 1.0 op_sel_hi:[1,0]
	v_log_f32_e32 v6, v6
	v_log_f32_e32 v7, v7
	v_pk_add_f32 v[0:1], v[16:17], 1.0 op_sel_hi:[1,0]
	v_pk_add_f32 v[2:3], v[2:3], 1.0 op_sel_hi:[1,0]
	v_log_f32_e32 v0, v0
	v_log_f32_e32 v1, v1
	v_exp_f32_e32 v18, v8
	v_exp_f32_e32 v19, v9
	v_log_f32_e32 v8, v2
	v_log_f32_e32 v9, v3
	v_pk_mul_f32 v[2:3], v[48:49], v[6:7] op_sel:[1,0]
	s_nop 0
	s_nop 0
	v_pk_mul_f32 v[0:1], v[48:49], v[0:1] op_sel:[1,0]
	s_nop 0
	s_nop 0
	v_cvt_pk_f16_f32 v3, v2, v3
	v_cvt_pk_f16_f32 v2, v0, v1
	v_pk_mul_f32 v[0:1], v[48:49], v[8:9] op_sel:[1,0]
	v_pk_mul_f32 v[4:5], v[48:49], v[4:5] op_sel:[1,0]
	s_nop 0
	s_nop 0
	s_nop 0
	s_nop 0
	v_cvt_pk_f16_f32 v1, v0, v1
	v_cvt_pk_f16_f32 v0, v4, v5
	v_pk_add_f32 v[4:5], v[18:19], 1.0 op_sel_hi:[1,0]
	v_exp_f32_e32 v6, v10
	v_exp_f32_e32 v7, v11
	v_exp_f32_e32 v8, v12
	v_exp_f32_e32 v9, v13
	v_exp_f32_e32 v10, v14
	v_exp_f32_e32 v11, v15
	v_pk_add_f32 v[8:9], v[8:9], 1.0 op_sel_hi:[1,0]
	v_pk_add_f32 v[10:11], v[10:11], 1.0 op_sel_hi:[1,0]
	v_pk_add_f32 v[6:7], v[6:7], 1.0 op_sel_hi:[1,0]
	v_log_f32_e32 v8, v8
	v_log_f32_e32 v9, v9
	v_log_f32_e32 v10, v10
	v_log_f32_e32 v11, v11
	ds_read_b128 v[12:15], v71
	v_log_f32_e32 v6, v6
	v_log_f32_e32 v7, v7
	v_log_f32_e32 v4, v4
	v_log_f32_e32 v5, v5
	v_pk_mul_f32 v[8:9], v[48:49], v[8:9] op_sel:[1,0]
	v_pk_mul_f32 v[10:11], v[48:49], v[10:11] op_sel:[1,0]
	v_cvt_pk_f16_f32 v118, v8, v9
	v_cvt_pk_f16_f32 v119, v10, v11
	v_pk_mul_f32 v[10:11], v[48:49], v[6:7] op_sel:[1,0]
	ds_read_b128 v[6:9], v71 offset:1024
	s_waitcnt lgkmcnt(1)
	v_mfma_f32_32x32x16_f16 v[16:31], v[0:3], v[12:15], 0
	s_nop 0
	s_nop 0
	v_mul_f32_e64 v4, v49, v4
	v_mul_f32_e64 v5, v49, v5
	v_exp_f32_e32 v32, v32
	v_exp_f32_e32 v33, v33
	s_nop 0
	s_nop 0
	v_cvt_pk_f16_f32 v117, v10, v11
	v_cvt_pk_f16_f32 v116, v4, v5
	v_exp_f32_e32 v36, v36
	v_exp_f32_e32 v37, v37
	v_pk_add_f32 v[32:33], v[32:33], 1.0 op_sel_hi:[1,0]
	s_waitcnt lgkmcnt(0)
	v_mfma_f32_32x32x16_f16 v[16:31], v[116:119], v[6:9], v[16:31]
	v_log_f32_e32 v54, v32
	v_log_f32_e32 v55, v33
	v_pk_add_f32 v[32:33], v[36:37], 1.0 op_sel_hi:[1,0]
	s_nop 0
	s_nop 0
	ds_read_b128 v[4:7], v71 offset:4096
	ds_read_b128 v[120:123], v71 offset:5120
	v_exp_f32_e32 v36, v38
	v_exp_f32_e32 v37, v39
	s_nop 0
	s_nop 0
	s_waitcnt lgkmcnt(1)
	v_mfma_f32_32x32x16_f16 v[0:15], v[0:3], v[4:7], 0
	v_exp_f32_e32 v34, v34
	v_exp_f32_e32 v35, v35
	v_pk_add_f32 v[36:37], v[36:37], 1.0 op_sel_hi:[1,0]
	v_log_f32_e32 v32, v32
	v_log_f32_e32 v33, v33
	v_log_f32_e32 v36, v36
	v_log_f32_e32 v37, v37
	v_pk_add_f32 v[34:35], v[34:35], 1.0 op_sel_hi:[1,0]
	v_pk_mul_f32 v[32:33], v[48:49], v[32:33] op_sel:[1,0]
	v_log_f32_e32 v38, v34
	v_log_f32_e32 v39, v35
	v_pk_mul_f32 v[34:35], v[48:49], v[36:37] op_sel:[1,0]
	v_pk_mul_f32 v[36:37], v[48:49], v[54:55] op_sel:[1,0]
	v_cvt_pk_f16_f32 v35, v34, v35
	v_cvt_pk_f16_f32 v34, v32, v33
	v_pk_mul_f32 v[32:33], v[48:49], v[38:39] op_sel:[1,0]
	s_waitcnt lgkmcnt(0)
	v_mfma_f32_32x32x16_f16 v[0:15], v[116:119], v[120:123], v[0:15]
	v_cvt_pk_f16_f32 v33, v32, v33
	v_cvt_pk_f16_f32 v32, v36, v37
	ds_read_b128 v[36:39], v71 offset:2048
	ds_read_b128 v[116:119], v71 offset:3072
	s_nop 0
	s_nop 0
	v_exp_f32_e32 v55, v44
	v_exp_f32_e32 v115, v45
	s_waitcnt lgkmcnt(1)
	v_mfma_f32_32x32x16_f16 v[16:31], v[32:35], v[36:39], v[16:31]
	ds_read_b128 v[36:39], v71 offset:6144
	v_exp_f32_e32 v44, v40
	v_exp_f32_e32 v45, v41
	v_exp_f32_e32 v52, v42
	v_exp_f32_e32 v54, v43
	ds_read_b128 v[40:43], v71 offset:7168
	s_nop 0
	s_waitcnt lgkmcnt(1)
	v_mfma_f32_32x32x16_f16 v[0:15], v[32:35], v[36:39], v[0:15]
	v_pk_add_f32 v[34:35], v[44:45], 1.0 op_sel_hi:[1,0]
	s_nop 0
	s_nop 0
	s_nop 0
	s_nop 0
	v_log_f32_e32 v36, v34
	v_log_f32_e32 v37, v35
	v_exp_f32_e32 v34, v46
	v_exp_f32_e32 v35, v47
	s_nop 0
	s_nop 0
	v_add_f32_e64 v32, v55, 1.0
	v_add_f32_e64 v33, v115, 1.0
	v_pk_add_f32 v[34:35], v[34:35], 1.0 op_sel_hi:[1,0]
	v_log_f32_e32 v32, v32
	v_log_f32_e32 v33, v33
	v_log_f32_e32 v34, v34
	v_log_f32_e32 v35, v35
	v_add_f32_e64 v38, v52, 1.0
	v_add_f32_e64 v39, v54, 1.0
	v_pk_mul_f32 v[32:33], v[48:49], v[32:33] op_sel:[1,0]
	v_log_f32_e32 v38, v38
	v_log_f32_e32 v39, v39
	v_pk_mul_f32 v[34:35], v[48:49], v[34:35] op_sel:[1,0]
	v_pk_mul_f32 v[36:37], v[48:49], v[36:37] op_sel:[1,0]
	v_cvt_pk_f16_f32 v35, v34, v35
	v_cvt_pk_f16_f32 v34, v32, v33
	v_pk_mul_f32 v[32:33], v[48:49], v[38:39] op_sel:[1,0]
	v_mov_b32_e32 v54, v53
	v_cvt_pk_f16_f32 v33, v32, v33
	v_cvt_pk_f16_f32 v32, v36, v37
	v_cvt_f16_f32_e32 v36, v49
	v_mov_b32_e32 v55, v53
	v_mfma_f32_32x32x16_f16 v[16:31], v[32:35], v[116:119], v[16:31]
	v_cmp_ne_u32_sdwa s[20:21], v95, v50 src0_sel:DWORD src1_sel:WORD_1
	v_cmp_ne_u32_sdwa s[18:19], v99, v50 src0_sel:WORD_1 src1_sel:WORD_1
	s_bitcmp1_b32 s20, 0
	v_cmp_lt_i32_e64 s[2:3], s13, v64
	s_cselect_b64 s[20:21], -1, 0
	s_bitcmp0_b32 s18, 0
	s_waitcnt lgkmcnt(0)
	v_mfma_f32_32x32x16_f16 v[0:15], v[32:35], v[40:43], v[0:15]
	v_cndmask_b32_e64 v32, 0, v36, s[0:1]
	v_pack_b32_f16 v52, v32, 0
	ds_read_b128 v[32:35], v72
	ds_read_b128 v[36:39], v72 offset:1024
	s_waitcnt vmcnt(0)
	s_waitcnt vmcnt(0)
	s_waitcnt lgkmcnt(1)
	v_mfma_f32_32x32x16_f16 v[16:31], v[52:55], v[32:35], v[16:31]
	v_mov_b64_e32 v[32:33], 0
	s_nop 0
	s_waitcnt lgkmcnt(0)
	v_mfma_f32_32x32x16_f16 v[0:15], v[52:55], v[36:39], v[0:15]
	s_nop 11
	v_permlane32_swap_b32_e32 v16, v0
	v_permlane32_swap_b32_e32 v17, v1
	v_permlane32_swap_b32_e32 v18, v2
	v_permlane32_swap_b32_e32 v19, v3
	v_permlane32_swap_b32_e32 v20, v4
	v_permlane32_swap_b32_e32 v21, v5
	v_permlane32_swap_b32_e32 v22, v6
	v_permlane32_swap_b32_e32 v23, v7
	v_permlane32_swap_b32_e32 v24, v8
	v_permlane32_swap_b32_e32 v25, v9
	v_permlane32_swap_b32_e32 v26, v10
	v_permlane32_swap_b32_e32 v27, v11
	v_permlane32_swap_b32_e32 v28, v12
	v_permlane32_swap_b32_e32 v29, v13
	v_permlane32_swap_b32_e32 v30, v14
	v_permlane32_swap_b32_e32 v31, v15
	v_fma_mix_f32 v32, v16, v112, v32 op_sel:[0,1,0] op_sel_hi:[0,1,0]
	v_fma_mix_f32 v33, v16, v112, v33 op_sel_hi:[0,1,0]
	s_cbranch_scc1 .LBB4_13
	v_readlane_b32 s10, v50, 0
	s_bfe_u32 s19, s10, 0x80008
	v_lshl_or_b32 v16, s19, 7, v73
	ds_read_u16 v16, v16
	s_bfe_u32 s10, s10, 0x100010
	s_lshl_b32 s10, s10, 8
	s_add_u32 s58, s60, s10
	s_addc_u32 s59, s61, 0
	s_cmp_lg_u64 s[20:21], 0
	s_cselect_b32 s58, s58, s62
	s_cselect_b32 s59, s59, s63
	s_nop 0
	s_waitcnt lgkmcnt(0)
	v_fma_mix_f32 v16, v16, v33, v32 op_sel_hi:[1,0,0]
	s_nop 0
	s_mov_b64 s[20:21], -1
	v_mov_b64_e32 v[32:33], 0
	s_nop 0
	global_store_dword v79, v16, s[58:59] sc1
